# P6 X1 stores nt (alone)
# baseline (speedup 1.0000x reference)
.LBB0_847:
	v_lshl_add_u32 v130, s38, 8, v1
	v_ashrrev_i32_e32 v131, 31, v130
	s_lshl_b32 s40, s34, 8
	v_lshlrev_b64 v[130:131], 10, v[130:131]
	s_ashr_i32 s41, s40, 31
	v_lshl_add_u64 v[226:227], v[130:131], 0, s[40:41]
	v_or_b32_e32 v226, v226, v202
	v_lshl_add_u64 v[178:179], v[226:227], 2, s[36:37]
	global_load_dwordx4 v[208:211], v[178:179], off
	global_load_dwordx4 v[212:215], v[178:179], off offset:16
	s_mov_b64 s[40:41], 0x10000
	v_add_co_u32_e32 v180, vcc, s61, v178
	v_lshl_add_u64 v[130:131], v[178:179], 0, s[40:41]
	s_nop 0
	v_addc_co_u32_e32 v181, vcc, 0, v179, vcc
	s_mov_b32 s23, 0x20000
	global_load_dwordx4 v[216:219], v[180:181], off
	global_load_dwordx4 v[222:225], v[130:131], off offset:16
	v_add_co_u32_e32 v182, vcc, s23, v178
	s_mov_b64 s[40:41], 0x20000
	s_nop 0
	v_addc_co_u32_e32 v183, vcc, 0, v179, vcc
	global_load_dwordx4 v[162:165], v[182:183], off
	v_lshl_add_u64 v[130:131], v[178:179], 0, s[40:41]
	s_mov_b32 s23, 0x30000
	global_load_dwordx4 v[150:153], v[130:131], off offset:16
	v_add_co_u32_e32 v184, vcc, s23, v178
	s_mov_b64 s[42:43], 0x30000
	s_nop 0
	v_addc_co_u32_e32 v185, vcc, 0, v179, vcc
	s_mov_b32 s25, 0x80000
	v_lshl_add_u64 v[130:131], v[178:179], 0, s[42:43]
	global_load_dwordx4 v[166:169], v[184:185], off
	global_load_dwordx4 v[154:157], v[130:131], off offset:16
	s_mov_b64 s[40:41], 0x80000
	v_add_co_u32_e32 v186, vcc, s25, v178
	v_lshl_add_u64 v[130:131], v[178:179], 0, s[40:41]
	s_nop 0
	v_addc_co_u32_e32 v187, vcc, 0, v179, vcc
	s_mov_b32 s23, 0x90000
	global_load_dwordx4 v[174:177], v[186:187], off
	global_load_dwordx4 v[170:173], v[130:131], off offset:16
	v_add_co_u32_e32 v192, vcc, s23, v178
	s_mov_b64 s[42:43], 0x90000
	s_nop 0
	v_addc_co_u32_e32 v193, vcc, 0, v179, vcc
	s_mov_b32 s34, 0xa0000
	v_lshl_add_u64 v[130:131], v[178:179], 0, s[42:43]
	global_load_dwordx4 v[158:161], v[192:193], off
	global_load_dwordx4 v[146:149], v[130:131], off offset:16
	v_add_co_u32_e32 v190, vcc, s34, v178
	s_mov_b64 s[44:45], 0xa0000
	s_mov_b32 s25, 0xb0000
	v_addc_co_u32_e32 v191, vcc, 0, v179, vcc
	v_lshl_add_u64 v[132:133], v[178:179], 0, s[44:45]
	v_add_co_u32_e32 v188, vcc, s25, v178
	global_load_dwordx4 v[142:145], v[190:191], off
	global_load_dwordx4 v[138:141], v[132:133], off offset:16
	s_mov_b64 s[40:41], 0xb0000
	v_addc_co_u32_e32 v189, vcc, 0, v179, vcc
	v_lshl_add_u64 v[228:229], v[178:179], 0, s[40:41]
	global_load_dwordx4 v[134:137], v[188:189], off
	global_load_dwordx4 v[130:133], v[228:229], off offset:16
	s_mov_b32 s23, 0x58000
	s_waitcnt vmcnt(0)
	v_pk_add_f32 v[228:229], v[128:129], v[210:211]
	v_pk_add_f32 v[230:231], v[126:127], v[208:209]
	v_pk_add_f32 v[232:233], v[124:125], v[214:215]
	v_pk_add_f32 v[214:215], v[122:123], v[212:213]
	v_lshlrev_b64 v[208:209], 1, v[226:227]
	v_lshl_add_u64 v[210:211], s[2:3], 0, v[208:209]
	v_cvt_pk_bf16_f32 v212, v230, v231
	v_cvt_pk_bf16_f32 v213, v228, v229
	v_cvt_pk_bf16_f32 v214, v214, v215
	v_cvt_pk_bf16_f32 v215, v232, v233
	global_store_dwordx4 v[210:211], v[212:215], off nt
	v_or_b32_e32 v208, 0x100, v208
	v_pk_add_f32 v[162:163], v[110:111], v[162:163]
	v_pk_add_f32 v[214:215], v[120:121], v[218:219]
	v_pk_add_f32 v[212:213], v[118:119], v[216:217]
	v_pk_add_f32 v[216:217], v[116:117], v[224:225]
	v_pk_add_f32 v[218:219], v[114:115], v[222:223]
	v_cvt_pk_bf16_f32 v212, v212, v213
	v_cvt_pk_bf16_f32 v213, v214, v215
	v_cvt_pk_bf16_f32 v215, v216, v217
	v_add_co_u32_e32 v216, vcc, s65, v210
	v_cvt_pk_bf16_f32 v214, v218, v219
	s_nop 0
	v_addc_co_u32_e32 v217, vcc, 0, v211, vcc
	global_store_dwordx4 v[216:217], v[212:215], off nt
	v_pk_add_f32 v[164:165], v[112:113], v[164:165]
	v_pk_add_f32 v[154:155], v[98:99], v[154:155]
	v_pk_add_f32 v[212:213], v[108:109], v[152:153]
	v_pk_add_f32 v[152:153], v[106:107], v[150:151]
	v_cvt_pk_bf16_f32 v150, v162, v163
	v_add_co_u32_e32 v162, vcc, s61, v210
	v_cvt_pk_bf16_f32 v151, v164, v165
	v_cvt_pk_bf16_f32 v152, v152, v153
	v_cvt_pk_bf16_f32 v153, v212, v213
	v_addc_co_u32_e32 v163, vcc, 0, v211, vcc
	global_store_dwordx4 v[162:163], v[150:153], off nt
	v_pk_add_f32 v[156:157], v[100:101], v[156:157]
	v_pk_add_f32 v[142:143], v[46:47], v[142:143]
	v_pk_add_f32 v[152:153], v[104:105], v[168:169]
	v_pk_add_f32 v[150:151], v[102:103], v[166:167]
	v_pk_add_f32 v[144:145], v[48:49], v[144:145]
	v_cvt_pk_bf16_f32 v150, v150, v151
	v_cvt_pk_bf16_f32 v151, v152, v153
	v_cvt_pk_bf16_f32 v152, v154, v155
	v_add_co_u32_e32 v154, vcc, s64, v210
	v_cvt_pk_bf16_f32 v153, v156, v157
	s_nop 0
	v_addc_co_u32_e32 v155, vcc, 0, v211, vcc
	global_store_dwordx4 v[154:155], v[150:153], off nt
	v_pk_add_f32 v[154:155], v[60:61], v[172:173]
	v_pk_add_f32 v[156:157], v[58:59], v[170:171]
	v_pk_add_f32 v[152:153], v[64:65], v[176:177]
	v_pk_add_f32 v[150:151], v[62:63], v[174:175]
	v_pk_add_f32 v[134:135], v[38:39], v[134:135]
	v_cvt_pk_bf16_f32 v150, v150, v151
	v_cvt_pk_bf16_f32 v151, v152, v153
	v_cvt_pk_bf16_f32 v153, v154, v155
	v_add_co_u32_e32 v154, vcc, s66, v210
	v_cvt_pk_bf16_f32 v152, v156, v157
	s_nop 0
	v_addc_co_u32_e32 v155, vcc, 0, v211, vcc
	global_store_dwordx4 v[154:155], v[150:153], off nt
	v_pk_add_f32 v[154:155], v[52:53], v[148:149]
	v_pk_add_f32 v[148:149], v[50:51], v[146:147]
	v_pk_add_f32 v[150:151], v[56:57], v[160:161]
	v_pk_add_f32 v[152:153], v[54:55], v[158:159]
	v_cvt_pk_bf16_f32 v147, v150, v151
	v_add_co_u32_e32 v150, vcc, s67, v210
	v_cvt_pk_bf16_f32 v146, v152, v153
	v_cvt_pk_bf16_f32 v148, v148, v149
	v_cvt_pk_bf16_f32 v149, v154, v155
	v_addc_co_u32_e32 v151, vcc, 0, v211, vcc
	global_store_dwordx4 v[150:151], v[146:149], off nt
	v_pk_add_f32 v[136:137], v[40:41], v[136:137]
	v_lshl_add_u64 v[150:151], v[178:179], 0, s[10:11]
	v_pk_add_f32 v[146:147], v[44:45], v[140:141]
	v_pk_add_f32 v[140:141], v[42:43], v[138:139]
	v_cvt_pk_bf16_f32 v138, v142, v143
	v_add_co_u32_e32 v142, vcc, s68, v210
	v_cvt_pk_bf16_f32 v139, v144, v145
	v_cvt_pk_bf16_f32 v140, v140, v141
	v_cvt_pk_bf16_f32 v141, v146, v147
	v_addc_co_u32_e32 v143, vcc, 0, v211, vcc
	global_store_dwordx4 v[142:143], v[138:141], off nt
	v_lshl_add_u64 v[142:143], v[178:179], 0, s[8:9]
	v_lshl_add_u64 v[158:159], v[178:179], 0, s[12:13]
	v_pk_add_f32 v[138:139], v[36:37], v[132:133]
	v_pk_add_f32 v[132:133], v[34:35], v[130:131]
	v_cvt_pk_bf16_f32 v130, v134, v135
	v_add_co_u32_e32 v134, vcc, s23, v210
	v_cvt_pk_bf16_f32 v131, v136, v137
	v_cvt_pk_bf16_f32 v132, v132, v133
	v_cvt_pk_bf16_f32 v133, v138, v139
	v_addc_co_u32_e32 v135, vcc, 0, v211, vcc
	global_store_dwordx4 v[134:135], v[130:133], off nt
	global_load_dwordx4 v[130:133], v[178:179], off offset:512
	s_nop 0
	global_load_dwordx4 v[134:137], v[178:179], off offset:528
	global_load_dwordx4 v[138:141], v[180:181], off offset:512
	s_nop 0
	global_load_dwordx4 v[142:145], v[142:143], off offset:16
	s_nop 0
	global_load_dwordx4 v[146:149], v[182:183], off offset:512
	s_nop 0
	global_load_dwordx4 v[150:153], v[150:151], off offset:16
	s_nop 0
	global_load_dwordx4 v[154:157], v[184:185], off offset:512
	s_nop 0
	global_load_dwordx4 v[158:161], v[158:159], off offset:16
	s_nop 0
	global_load_dwordx4 v[162:165], v[186:187], off offset:512
	v_lshl_add_u64 v[166:167], v[178:179], 0, s[14:15]
	global_load_dwordx4 v[166:169], v[166:167], off offset:16
	s_nop 0
	global_load_dwordx4 v[170:173], v[192:193], off offset:512
	v_lshl_add_u64 v[174:175], v[178:179], 0, s[16:17]
	global_load_dwordx4 v[174:177], v[174:175], off offset:16
	v_lshl_add_u64 v[192:193], v[178:179], 0, s[18:19]
	global_load_dwordx4 v[180:183], v[190:191], off offset:512
	v_lshl_add_u64 v[178:179], v[178:179], 0, s[20:21]
	global_load_dwordx4 v[184:187], v[188:189], off offset:512
	s_nop 0
	global_load_dwordx4 v[188:191], v[192:193], off offset:16
	global_load_dwordx4 v[210:213], v[178:179], off offset:16
	v_lshl_add_u64 v[178:179], s[2:3], 0, v[208:209]
	s_waitcnt vmcnt(15)
	v_pk_add_f32 v[132:133], v[96:97], v[132:133]
	v_pk_add_f32 v[130:131], v[94:95], v[130:131]
	s_waitcnt vmcnt(14)
	v_pk_add_f32 v[136:137], v[92:93], v[136:137]
	v_pk_add_f32 v[134:135], v[90:91], v[134:135]
	v_cvt_pk_bf16_f32 v130, v130, v131
	v_cvt_pk_bf16_f32 v131, v132, v133
	v_cvt_pk_bf16_f32 v132, v134, v135
	v_cvt_pk_bf16_f32 v133, v136, v137
	global_store_dwordx4 v[178:179], v[130:133], off nt
	s_waitcnt vmcnt(13)
	v_pk_add_f32 v[134:135], v[84:85], v[144:145]
	v_pk_add_f32 v[136:137], v[82:83], v[142:143]
	v_pk_add_f32 v[132:133], v[88:89], v[140:141]
	v_pk_add_f32 v[130:131], v[86:87], v[138:139]
	s_nop 0
	v_cvt_pk_bf16_f32 v130, v130, v131
	v_cvt_pk_bf16_f32 v131, v132, v133
	v_cvt_pk_bf16_f32 v133, v134, v135
	v_add_co_u32_e32 v134, vcc, s65, v178
	v_cvt_pk_bf16_f32 v132, v136, v137
	s_nop 0
	v_addc_co_u32_e32 v135, vcc, 0, v179, vcc
	global_store_dwordx4 v[134:135], v[130:133], off nt
	s_waitcnt vmcnt(12)
	v_pk_add_f32 v[134:135], v[76:77], v[152:153]
	v_pk_add_f32 v[136:137], v[74:75], v[150:151]
	v_pk_add_f32 v[132:133], v[80:81], v[148:149]
	v_pk_add_f32 v[130:131], v[78:79], v[146:147]
	s_nop 0
	v_cvt_pk_bf16_f32 v130, v130, v131
	v_cvt_pk_bf16_f32 v131, v132, v133
	v_cvt_pk_bf16_f32 v133, v134, v135
	v_add_co_u32_e32 v134, vcc, s61, v178
	v_cvt_pk_bf16_f32 v132, v136, v137
	s_nop 0
	v_addc_co_u32_e32 v135, vcc, 0, v179, vcc
	global_store_dwordx4 v[134:135], v[130:133], off nt
	s_waitcnt vmcnt(11)
	v_pk_add_f32 v[134:135], v[68:69], v[160:161]
	v_pk_add_f32 v[136:137], v[66:67], v[158:159]
	v_pk_add_f32 v[132:133], v[72:73], v[156:157]
	v_pk_add_f32 v[130:131], v[70:71], v[154:155]
	s_nop 0
	v_cvt_pk_bf16_f32 v130, v130, v131
	v_cvt_pk_bf16_f32 v131, v132, v133
	v_cvt_pk_bf16_f32 v133, v134, v135
	v_add_co_u32_e32 v134, vcc, s64, v178
	v_cvt_pk_bf16_f32 v132, v136, v137
	s_nop 0
	v_addc_co_u32_e32 v135, vcc, 0, v179, vcc
	global_store_dwordx4 v[134:135], v[130:133], off nt
	s_waitcnt vmcnt(10)
	v_pk_add_f32 v[134:135], v[28:29], v[168:169]
	v_pk_add_f32 v[136:137], v[26:27], v[166:167]
	v_pk_add_f32 v[132:133], v[32:33], v[164:165]
	v_pk_add_f32 v[130:131], v[30:31], v[162:163]
	s_nop 0
	v_cvt_pk_bf16_f32 v130, v130, v131
	v_cvt_pk_bf16_f32 v131, v132, v133
	v_cvt_pk_bf16_f32 v133, v134, v135
	v_add_co_u32_e32 v134, vcc, s66, v178
	v_cvt_pk_bf16_f32 v132, v136, v137
	s_nop 0
	v_addc_co_u32_e32 v135, vcc, 0, v179, vcc
	global_store_dwordx4 v[134:135], v[130:133], off nt
	s_waitcnt vmcnt(9)
	v_pk_add_f32 v[134:135], v[20:21], v[176:177]
	v_pk_add_f32 v[136:137], v[18:19], v[174:175]
	v_pk_add_f32 v[132:133], v[24:25], v[172:173]
	v_pk_add_f32 v[130:131], v[22:23], v[170:171]
	s_nop 0
	v_cvt_pk_bf16_f32 v130, v130, v131
	v_cvt_pk_bf16_f32 v131, v132, v133
	v_cvt_pk_bf16_f32 v133, v134, v135
	v_add_co_u32_e32 v134, vcc, s67, v178
	v_cvt_pk_bf16_f32 v132, v136, v137
	s_nop 0
	v_addc_co_u32_e32 v135, vcc, 0, v179, vcc
	global_store_dwordx4 v[134:135], v[130:133], off nt
	s_waitcnt vmcnt(7)
	v_pk_add_f32 v[134:135], v[12:13], v[190:191]
	v_pk_add_f32 v[136:137], v[10:11], v[188:189]
	v_pk_add_f32 v[132:133], v[16:17], v[182:183]
	v_pk_add_f32 v[130:131], v[14:15], v[180:181]
	s_nop 0
	v_cvt_pk_bf16_f32 v130, v130, v131
	v_cvt_pk_bf16_f32 v131, v132, v133
	v_cvt_pk_bf16_f32 v133, v134, v135
	v_add_co_u32_e32 v134, vcc, s68, v178
	v_cvt_pk_bf16_f32 v132, v136, v137
	s_nop 0
	v_addc_co_u32_e32 v135, vcc, 0, v179, vcc
	global_store_dwordx4 v[134:135], v[130:133], off nt
	s_waitcnt vmcnt(7)
	v_pk_add_f32 v[134:135], v[4:5], v[212:213]
	v_pk_add_f32 v[136:137], v[2:3], v[210:211]
	v_pk_add_f32 v[132:133], v[8:9], v[186:187]
	v_pk_add_f32 v[130:131], v[6:7], v[184:185]
	s_nop 0
	v_cvt_pk_bf16_f32 v130, v130, v131
	v_cvt_pk_bf16_f32 v131, v132, v133
	v_cvt_pk_bf16_f32 v133, v134, v135
	v_add_co_u32_e32 v134, vcc, 0x58000, v178
	v_cvt_pk_bf16_f32 v132, v136, v137
	s_nop 0
	v_addc_co_u32_e32 v135, vcc, 0, v179, vcc
	s_andn2_b64 vcc, exec, s[28:29]
	s_mov_b64 s[28:29], -1
	global_store_dwordx4 v[134:135], v[130:133], off nt
	s_cbranch_vccnz .LBB0_832
	s_andn2_b64 vcc, exec, s[0:1]
	s_cbranch_vccnz .LBB0_831
	s_barrier
	s_branch .LBB0_831
